# all fp8 GEMM unit loops: the 128 accumulator-zeroing moves per unit removed; the first half-trip is a peeled copy whose MFMAs take C=0
# speedup vs baseline: 1.0145x; 1.0145x over previous
.LBB0_287:
	s_cmp_lg_u32 s16, 0
	s_cselect_b64 s[16:17], -1, 0
	s_add_u32 s13, s0, 0x100
	s_addc_u32 s53, s1, 0
	s_mov_b32 s54, -2
	s_mov_b64 s[18:19], 0
	v_add_u32_e32 v2, 0x10000, v218
	v_add_u32_e32 v6, 0x14000, v218
	ds_read_b128 v[26:29], v2
	ds_read_b128 v[30:33], v2 offset:1024
	ds_read_b128 v[18:21], v2 offset:2048
	ds_read_b128 v[22:25], v2 offset:3072
	ds_read_b128 v[10:13], v6
	ds_read_b128 v[14:17], v6 offset:1024
	ds_read_b128 v[2:5], v6 offset:2048
	ds_read_b128 v[6:9], v6 offset:3072
	s_add_u32 s22, s2, s18
	s_addc_u32 s23, s3, s19
	s_cmp_eq_u32 s18, 0
	s_cselect_b64 s[0:1], -1, 0
	ds_read_b128 v[58:61], v219
	ds_read_b128 v[62:65], v219 offset:1024
	ds_read_b128 v[50:53], v219 offset:2048
	ds_read_b128 v[54:57], v219 offset:3072
	ds_read_b128 v[42:45], v219 offset:4096
	ds_read_b128 v[46:49], v219 offset:5120
	ds_read_b128 v[34:37], v219 offset:6144
	ds_read_b128 v[38:41], v219 offset:7168
	s_and_b64 s[0:1], s[16:17], s[0:1]
	s_mov_b64 s[20:21], -1
	s_and_b64 vcc, exec, s[0:1]
	s_cbranch_vccnz .Lpeel_convin_291
	s_add_u32 s20, s22, 0x80
	s_addc_u32 s21, s23, 0
	s_mov_b32 m0, s44
	s_nop 0
	global_load_lds_dwordx4 v225, s[20:21]
	s_nop 0
	s_mov_b32 m0, s45
	s_nop 0
	global_load_lds_dwordx4 v226, s[20:21]
	s_waitcnt vmcnt(8)
	s_mov_b64 s[20:21], 0

.Lpeel_convin_293:
	s_xor_b64 s[24:25], s[0:1], -1
	s_add_u32 s22, s22, 0x100
	s_addc_u32 s23, s23, 0
	s_add_u32 s26, s13, s18
	s_addc_u32 s27, s53, s19
	s_cmpk_eq_i32 s18, 0x300
	s_cselect_b64 s[0:1], -1, 0
	s_waitcnt lgkmcnt(0)
	s_and_b64 s[20:21], s[0:1], exec
	v_cndmask_b32_e64 v227, v194, v220, s[0:1]
	s_cselect_b32 s23, s3, s23
	s_cselect_b32 s22, s2, s22
	v_cndmask_b32_e64 v228, v224, v221, s[0:1]
	s_cselect_b32 s21, s11, s27
	s_cselect_b32 s20, s10, s26
	s_barrier
	s_setprio 1
	s_waitcnt lgkmcnt(6)
	v_mfma_f32_16x16x128_f8f6f4 v[190:193], v[26:33], v[58:65], 0
	v_mfma_f32_16x16x128_f8f6f4 v[186:189], v[18:25], v[58:65], 0
	s_waitcnt lgkmcnt(4)
	v_mfma_f32_16x16x128_f8f6f4 v[178:181], v[26:33], v[50:57], 0
	v_mfma_f32_16x16x128_f8f6f4 v[170:173], v[18:25], v[50:57], 0
	s_waitcnt lgkmcnt(2)
	v_mfma_f32_16x16x128_f8f6f4 v[162:165], v[26:33], v[42:49], 0
	v_mfma_f32_16x16x128_f8f6f4 v[154:157], v[18:25], v[42:49], 0
	s_waitcnt lgkmcnt(0)
	v_mfma_f32_16x16x128_f8f6f4 v[146:149], v[26:33], v[34:41], 0
	v_mfma_f32_16x16x128_f8f6f4 v[138:141], v[18:25], v[34:41], 0
	s_setprio 0
	s_setprio 1
	v_mfma_f32_16x16x128_f8f6f4 v[182:185], v[10:17], v[58:65], 0
	v_mfma_f32_16x16x128_f8f6f4 v[174:177], v[2:9], v[58:65], 0
	v_mfma_f32_16x16x128_f8f6f4 v[166:169], v[10:17], v[50:57], 0
	v_mfma_f32_16x16x128_f8f6f4 v[158:161], v[2:9], v[50:57], 0
	v_mfma_f32_16x16x128_f8f6f4 v[150:153], v[10:17], v[42:49], 0
	v_mfma_f32_16x16x128_f8f6f4 v[142:145], v[2:9], v[42:49], 0
	v_mfma_f32_16x16x128_f8f6f4 v[134:137], v[10:17], v[34:41], 0
	v_mfma_f32_16x16x128_f8f6f4 v[130:133], v[2:9], v[34:41], 0
	s_setprio 0
	s_barrier
	ds_read_b128 v[58:61], v219 offset:16384
	ds_read_b128 v[62:65], v219 offset:17408
	ds_read_b128 v[50:53], v219 offset:18432
	ds_read_b128 v[54:57], v219 offset:19456
	ds_read_b128 v[42:45], v219 offset:20480
	ds_read_b128 v[46:49], v219 offset:21504
	ds_read_b128 v[34:37], v219 offset:22528
	ds_read_b128 v[38:41], v219 offset:23552
	s_mov_b32 m0, s29
	s_nop 0
	global_load_lds_dwordx4 v211, s[20:21]
	s_nop 0
	s_mov_b32 m0, s30
	s_nop 0
	global_load_lds_dwordx4 v214, s[20:21]
	s_add_u32 s26, s20, 0x20000
	s_addc_u32 s27, s21, 0
	s_mov_b32 m0, s31
	s_nop 0
	global_load_lds_dwordx4 v211, s[26:27]
	s_and_b64 vcc, exec, s[24:25]
	s_mov_b32 m0, s34
	s_nop 0
	global_load_lds_dwordx4 v214, s[26:27]
	s_mov_b32 m0, s28
	s_nop 0
	global_load_lds_dwordx4 v227, s[22:23]
	s_nop 0
	s_mov_b32 m0, s35
	s_nop 0
	global_load_lds_dwordx4 v228, s[22:23]
	s_mov_b64 s[26:27], -1
	s_cbranch_vccz .Lpeel_convin_295
	s_waitcnt vmcnt(8)
	s_mov_b64 s[26:27], 0

.Lpeel_convin_297:
	s_waitcnt lgkmcnt(0)
	v_cndmask_b32_e64 v229, v225, v222, s[0:1]
	v_cndmask_b32_e64 v230, v226, v223, s[0:1]
	s_barrier
	s_setprio 1
	s_waitcnt lgkmcnt(6)
	v_mfma_f32_16x16x128_f8f6f4 v[126:129], v[26:33], v[58:65], 0
	v_mfma_f32_16x16x128_f8f6f4 v[122:125], v[18:25], v[58:65], 0
	s_waitcnt lgkmcnt(4)
	v_mfma_f32_16x16x128_f8f6f4 v[114:117], v[26:33], v[50:57], 0
	v_mfma_f32_16x16x128_f8f6f4 v[106:109], v[18:25], v[50:57], 0
	s_waitcnt lgkmcnt(2)
	v_mfma_f32_16x16x128_f8f6f4 v[82:85], v[26:33], v[42:49], 0
	v_mfma_f32_16x16x128_f8f6f4 v[78:81], v[18:25], v[42:49], 0
	s_waitcnt lgkmcnt(0)
	v_mfma_f32_16x16x128_f8f6f4 v[70:73], v[26:33], v[34:41], 0
	v_mfma_f32_16x16x128_f8f6f4 v[66:69], v[18:25], v[34:41], 0
	s_setprio 0
	s_setprio 1
	v_mfma_f32_16x16x128_f8f6f4 v[118:121], v[10:17], v[58:65], 0
	v_mfma_f32_16x16x128_f8f6f4 v[110:113], v[2:9], v[58:65], 0
	v_mfma_f32_16x16x128_f8f6f4 v[86:89], v[10:17], v[50:57], 0
	v_mfma_f32_16x16x128_f8f6f4 v[74:77], v[2:9], v[50:57], 0
	v_mfma_f32_16x16x128_f8f6f4 v[102:105], v[10:17], v[42:49], 0
	v_mfma_f32_16x16x128_f8f6f4 v[98:101], v[2:9], v[42:49], 0
	v_mfma_f32_16x16x128_f8f6f4 v[94:97], v[10:17], v[34:41], 0
	v_mfma_f32_16x16x128_f8f6f4 v[90:93], v[2:9], v[34:41], 0
	s_setprio 0
	s_barrier
	s_branch .Lmid_convin

.Lmid_convin:
	v_add_u32_e32 v2, 0x18000, v218
	v_add_u32_e32 v6, 0x1c000, v218
	ds_read_b128 v[26:29], v2
	ds_read_b128 v[30:33], v2 offset:1024
	ds_read_b128 v[18:21], v2 offset:2048
	ds_read_b128 v[22:25], v2 offset:3072
	ds_read_b128 v[10:13], v6
	ds_read_b128 v[14:17], v6 offset:1024
	ds_read_b128 v[2:5], v6 offset:2048
	ds_read_b128 v[6:9], v6 offset:3072
	ds_read_b128 v[58:61], v219 offset:32768
	ds_read_b128 v[62:65], v219 offset:33792
	ds_read_b128 v[50:53], v219 offset:34816
	ds_read_b128 v[54:57], v219 offset:35840
	ds_read_b128 v[42:45], v219 offset:36864
	ds_read_b128 v[46:49], v219 offset:37888
	ds_read_b128 v[34:37], v219 offset:38912
	ds_read_b128 v[38:41], v219 offset:39936
	s_mov_b32 m0, s36
	s_nop 0
	global_load_lds_dwordx4 v229, s[22:23]
	s_and_b64 vcc, exec, s[24:25]
	s_mov_b32 m0, s37
	s_nop 0
	global_load_lds_dwordx4 v230, s[22:23]
	s_mov_b64 s[0:1], -1
	s_cbranch_vccz .LBB0_299
	s_waitcnt vmcnt(8)
	s_mov_b64 s[0:1], 0

.LBB0_564:
	s_cmp_lg_u32 s16, 0
	s_cselect_b64 s[16:17], -1, 0
	s_add_u32 s13, s0, 0x100
	s_addc_u32 s53, s1, 0
	s_mov_b32 s54, -2
	s_mov_b64 s[18:19], 0
	v_add_u32_e32 v2, 0x10000, v216
	v_add_u32_e32 v6, 0x14000, v216
	ds_read_b128 v[26:29], v2
	ds_read_b128 v[30:33], v2 offset:1024
	ds_read_b128 v[18:21], v2 offset:2048
	ds_read_b128 v[22:25], v2 offset:3072
	ds_read_b128 v[10:13], v6
	ds_read_b128 v[14:17], v6 offset:1024
	ds_read_b128 v[2:5], v6 offset:2048
	ds_read_b128 v[6:9], v6 offset:3072
	s_add_u32 s22, s2, s18
	s_addc_u32 s23, s3, s19
	s_cmp_eq_u32 s18, 0
	s_cselect_b64 s[0:1], -1, 0
	ds_read_b128 v[58:61], v217
	ds_read_b128 v[62:65], v217 offset:1024
	ds_read_b128 v[50:53], v217 offset:2048
	ds_read_b128 v[54:57], v217 offset:3072
	ds_read_b128 v[42:45], v217 offset:4096
	ds_read_b128 v[46:49], v217 offset:5120
	ds_read_b128 v[34:37], v217 offset:6144
	ds_read_b128 v[38:41], v217 offset:7168
	s_and_b64 s[0:1], s[16:17], s[0:1]
	s_mov_b64 s[20:21], -1
	s_and_b64 vcc, exec, s[0:1]
	s_cbranch_vccnz .Lpeel_swain_568
	s_add_u32 s20, s22, 0x80
	s_addc_u32 s21, s23, 0
	s_mov_b32 m0, s44
	s_nop 0
	global_load_lds_dwordx4 v224, s[20:21]
	s_nop 0
	s_mov_b32 m0, s45
	s_nop 0
	global_load_lds_dwordx4 v225, s[20:21]
	s_waitcnt vmcnt(8)
	s_mov_b64 s[20:21], 0

.Lpeel_swain_570:
	s_xor_b64 s[24:25], s[0:1], -1
	s_add_u32 s22, s22, 0x100
	s_addc_u32 s23, s23, 0
	s_add_u32 s26, s13, s18
	s_addc_u32 s27, s53, s19
	s_cmpk_eq_i32 s18, 0x300
	s_cselect_b64 s[0:1], -1, 0
	s_waitcnt lgkmcnt(0)
	s_and_b64 s[20:21], s[0:1], exec
	v_cndmask_b32_e64 v226, v222, v218, s[0:1]
	s_cselect_b32 s23, s3, s23
	s_cselect_b32 s22, s2, s22
	v_cndmask_b32_e64 v227, v223, v219, s[0:1]
	s_cselect_b32 s21, s11, s27
	s_cselect_b32 s20, s10, s26
	s_barrier
	s_setprio 1
	s_waitcnt lgkmcnt(6)
	v_mfma_f32_16x16x128_f8f6f4 v[190:193], v[26:33], v[58:65], 0
	v_mfma_f32_16x16x128_f8f6f4 v[186:189], v[18:25], v[58:65], 0
	s_waitcnt lgkmcnt(4)
	v_mfma_f32_16x16x128_f8f6f4 v[178:181], v[26:33], v[50:57], 0
	v_mfma_f32_16x16x128_f8f6f4 v[170:173], v[18:25], v[50:57], 0
	s_waitcnt lgkmcnt(2)
	v_mfma_f32_16x16x128_f8f6f4 v[162:165], v[26:33], v[42:49], 0
	v_mfma_f32_16x16x128_f8f6f4 v[154:157], v[18:25], v[42:49], 0
	s_waitcnt lgkmcnt(0)
	v_mfma_f32_16x16x128_f8f6f4 v[146:149], v[26:33], v[34:41], 0
	v_mfma_f32_16x16x128_f8f6f4 v[138:141], v[18:25], v[34:41], 0
	s_setprio 0
	s_setprio 1
	v_mfma_f32_16x16x128_f8f6f4 v[182:185], v[10:17], v[58:65], 0
	v_mfma_f32_16x16x128_f8f6f4 v[174:177], v[2:9], v[58:65], 0
	v_mfma_f32_16x16x128_f8f6f4 v[166:169], v[10:17], v[50:57], 0
	v_mfma_f32_16x16x128_f8f6f4 v[158:161], v[2:9], v[50:57], 0
	v_mfma_f32_16x16x128_f8f6f4 v[150:153], v[10:17], v[42:49], 0
	v_mfma_f32_16x16x128_f8f6f4 v[142:145], v[2:9], v[42:49], 0
	v_mfma_f32_16x16x128_f8f6f4 v[134:137], v[10:17], v[34:41], 0
	v_mfma_f32_16x16x128_f8f6f4 v[130:133], v[2:9], v[34:41], 0
	s_setprio 0
	s_barrier
	ds_read_b128 v[58:61], v217 offset:16384
	ds_read_b128 v[62:65], v217 offset:17408
	ds_read_b128 v[50:53], v217 offset:18432
	ds_read_b128 v[54:57], v217 offset:19456
	ds_read_b128 v[42:45], v217 offset:20480
	ds_read_b128 v[46:49], v217 offset:21504
	ds_read_b128 v[34:37], v217 offset:22528
	ds_read_b128 v[38:41], v217 offset:23552
	s_mov_b32 m0, s29
	s_nop 0
	global_load_lds_dwordx4 v210, s[20:21]
	s_nop 0
	s_mov_b32 m0, s30
	s_nop 0
	global_load_lds_dwordx4 v213, s[20:21]
	s_add_u32 s26, s20, 0x20000
	s_addc_u32 s27, s21, 0
	s_mov_b32 m0, s31
	s_nop 0
	global_load_lds_dwordx4 v210, s[26:27]
	s_and_b64 vcc, exec, s[24:25]
	s_mov_b32 m0, s34
	s_nop 0
	global_load_lds_dwordx4 v213, s[26:27]
	s_mov_b32 m0, s28
	s_nop 0
	global_load_lds_dwordx4 v226, s[22:23]
	s_nop 0
	s_mov_b32 m0, s35
	s_nop 0
	global_load_lds_dwordx4 v227, s[22:23]
	s_mov_b64 s[26:27], -1
	s_cbranch_vccz .Lpeel_swain_572
	s_waitcnt vmcnt(8)
	s_mov_b64 s[26:27], 0

.Lpeel_swain_574:
	s_waitcnt lgkmcnt(0)
	v_cndmask_b32_e64 v228, v224, v220, s[0:1]
	v_cndmask_b32_e64 v229, v225, v221, s[0:1]
	s_barrier
	s_setprio 1
	s_waitcnt lgkmcnt(6)
	v_mfma_f32_16x16x128_f8f6f4 v[126:129], v[26:33], v[58:65], 0
	v_mfma_f32_16x16x128_f8f6f4 v[122:125], v[18:25], v[58:65], 0
	s_waitcnt lgkmcnt(4)
	v_mfma_f32_16x16x128_f8f6f4 v[114:117], v[26:33], v[50:57], 0
	v_mfma_f32_16x16x128_f8f6f4 v[98:101], v[18:25], v[50:57], 0
	s_waitcnt lgkmcnt(2)
	v_mfma_f32_16x16x128_f8f6f4 v[82:85], v[26:33], v[42:49], 0
	v_mfma_f32_16x16x128_f8f6f4 v[78:81], v[18:25], v[42:49], 0
	s_waitcnt lgkmcnt(0)
	v_mfma_f32_16x16x128_f8f6f4 v[70:73], v[26:33], v[34:41], 0
	v_mfma_f32_16x16x128_f8f6f4 v[66:69], v[18:25], v[34:41], 0
	s_setprio 0
	s_setprio 1
	v_mfma_f32_16x16x128_f8f6f4 v[118:121], v[10:17], v[58:65], 0
	v_mfma_f32_16x16x128_f8f6f4 v[102:105], v[2:9], v[58:65], 0
	v_mfma_f32_16x16x128_f8f6f4 v[86:89], v[10:17], v[50:57], 0
	v_mfma_f32_16x16x128_f8f6f4 v[74:77], v[2:9], v[50:57], 0
	v_mfma_f32_16x16x128_f8f6f4 v[110:113], v[10:17], v[42:49], 0
	v_mfma_f32_16x16x128_f8f6f4 v[106:109], v[2:9], v[42:49], 0
	v_mfma_f32_16x16x128_f8f6f4 v[94:97], v[10:17], v[34:41], 0
	v_mfma_f32_16x16x128_f8f6f4 v[90:93], v[2:9], v[34:41], 0
	s_setprio 0
	s_barrier
	s_branch .Lmid_swain

.Lmid_swain:
	v_add_u32_e32 v2, 0x18000, v216
	v_add_u32_e32 v6, 0x1c000, v216
	ds_read_b128 v[26:29], v2
	ds_read_b128 v[30:33], v2 offset:1024
	ds_read_b128 v[18:21], v2 offset:2048
	ds_read_b128 v[22:25], v2 offset:3072
	ds_read_b128 v[10:13], v6
	ds_read_b128 v[14:17], v6 offset:1024
	ds_read_b128 v[2:5], v6 offset:2048
	ds_read_b128 v[6:9], v6 offset:3072
	ds_read_b128 v[58:61], v217 offset:32768
	ds_read_b128 v[62:65], v217 offset:33792
	ds_read_b128 v[50:53], v217 offset:34816
	ds_read_b128 v[54:57], v217 offset:35840
	ds_read_b128 v[42:45], v217 offset:36864
	ds_read_b128 v[46:49], v217 offset:37888
	ds_read_b128 v[34:37], v217 offset:38912
	ds_read_b128 v[38:41], v217 offset:39936
	s_mov_b32 m0, s36
	s_nop 0
	global_load_lds_dwordx4 v228, s[22:23]
	s_and_b64 vcc, exec, s[24:25]
	s_mov_b32 m0, s37
	s_nop 0
	global_load_lds_dwordx4 v229, s[22:23]
	s_mov_b64 s[0:1], -1
	s_cbranch_vccz .LBB0_576
	s_waitcnt vmcnt(8)
	s_mov_b64 s[0:1], 0

.LBB0_598:
	s_cmp_lg_u32 s16, 0
	s_cselect_b64 s[16:17], -1, 0
	s_add_u32 s13, s0, 0x100
	s_waitcnt vmcnt(13)
	s_addc_u32 s52, s1, 0
	s_mov_b32 s53, -2
	s_mov_b64 s[18:19], 0
	s_waitcnt vmcnt(1)
	s_waitcnt vmcnt(0)
	v_add_u32_e32 v2, 0x10000, v216
	v_add_u32_e32 v6, 0x14000, v216
	ds_read_b128 v[26:29], v2
	ds_read_b128 v[30:33], v2 offset:1024
	ds_read_b128 v[18:21], v2 offset:2048
	ds_read_b128 v[22:25], v2 offset:3072
	ds_read_b128 v[10:13], v6
	ds_read_b128 v[14:17], v6 offset:1024
	ds_read_b128 v[2:5], v6 offset:2048
	ds_read_b128 v[6:9], v6 offset:3072
	s_add_u32 s22, s2, s18
	s_addc_u32 s23, s3, s19
	s_cmp_eq_u32 s18, 0
	s_cselect_b64 s[0:1], -1, 0
	ds_read_b128 v[58:61], v217
	ds_read_b128 v[62:65], v217 offset:1024
	ds_read_b128 v[50:53], v217 offset:2048
	ds_read_b128 v[54:57], v217 offset:3072
	ds_read_b128 v[42:45], v217 offset:4096
	ds_read_b128 v[46:49], v217 offset:5120
	ds_read_b128 v[34:37], v217 offset:6144
	ds_read_b128 v[38:41], v217 offset:7168
	s_and_b64 s[0:1], s[16:17], s[0:1]
	s_mov_b64 s[20:21], -1
	s_and_b64 vcc, exec, s[0:1]
	s_cbranch_vccnz .Lpeel_hgrnin_602
	s_add_u32 s20, s22, 0x80
	s_addc_u32 s21, s23, 0
	s_mov_b32 m0, s44
	s_nop 0
	global_load_lds_dwordx4 v224, s[20:21]
	s_nop 0
	s_mov_b32 m0, s45
	s_nop 0
	global_load_lds_dwordx4 v225, s[20:21]
	s_waitcnt vmcnt(8)
	s_mov_b64 s[20:21], 0

.Lpeel_hgrnin_604:
	s_xor_b64 s[24:25], s[0:1], -1
	s_add_u32 s22, s22, 0x100
	s_addc_u32 s23, s23, 0
	s_add_u32 s26, s13, s18
	s_addc_u32 s27, s52, s19
	s_cmpk_eq_i32 s18, 0x300
	s_cselect_b64 s[0:1], -1, 0
	s_waitcnt lgkmcnt(0)
	s_and_b64 s[20:21], s[0:1], exec
	v_cndmask_b32_e64 v226, v222, v218, s[0:1]
	s_cselect_b32 s23, s3, s23
	s_cselect_b32 s22, s2, s22
	v_cndmask_b32_e64 v227, v223, v219, s[0:1]
	s_cselect_b32 s21, s11, s27
	s_cselect_b32 s20, s10, s26
	s_barrier
	s_setprio 1
	s_waitcnt lgkmcnt(6)
	v_mfma_f32_16x16x128_f8f6f4 v[190:193], v[26:33], v[58:65], 0
	v_mfma_f32_16x16x128_f8f6f4 v[186:189], v[18:25], v[58:65], 0
	s_waitcnt lgkmcnt(4)
	v_mfma_f32_16x16x128_f8f6f4 v[174:177], v[26:33], v[50:57], 0
	v_mfma_f32_16x16x128_f8f6f4 v[170:173], v[18:25], v[50:57], 0
	s_waitcnt lgkmcnt(2)
	v_mfma_f32_16x16x128_f8f6f4 v[158:161], v[26:33], v[42:49], 0
	v_mfma_f32_16x16x128_f8f6f4 v[154:157], v[18:25], v[42:49], 0
	s_waitcnt lgkmcnt(0)
	v_mfma_f32_16x16x128_f8f6f4 v[142:145], v[26:33], v[34:41], 0
	v_mfma_f32_16x16x128_f8f6f4 v[138:141], v[18:25], v[34:41], 0
	s_setprio 0
	s_setprio 1
	v_mfma_f32_16x16x128_f8f6f4 v[182:185], v[10:17], v[58:65], 0
	v_mfma_f32_16x16x128_f8f6f4 v[178:181], v[2:9], v[58:65], 0
	v_mfma_f32_16x16x128_f8f6f4 v[166:169], v[10:17], v[50:57], 0
	v_mfma_f32_16x16x128_f8f6f4 v[162:165], v[2:9], v[50:57], 0
	v_mfma_f32_16x16x128_f8f6f4 v[150:153], v[10:17], v[42:49], 0
	v_mfma_f32_16x16x128_f8f6f4 v[146:149], v[2:9], v[42:49], 0
	v_mfma_f32_16x16x128_f8f6f4 v[134:137], v[10:17], v[34:41], 0
	v_mfma_f32_16x16x128_f8f6f4 v[130:133], v[2:9], v[34:41], 0
	s_setprio 0
	s_barrier
	ds_read_b128 v[58:61], v217 offset:16384
	ds_read_b128 v[62:65], v217 offset:17408
	ds_read_b128 v[50:53], v217 offset:18432
	ds_read_b128 v[54:57], v217 offset:19456
	ds_read_b128 v[42:45], v217 offset:20480
	ds_read_b128 v[46:49], v217 offset:21504
	ds_read_b128 v[34:37], v217 offset:22528
	ds_read_b128 v[38:41], v217 offset:23552
	s_mov_b32 m0, s29
	s_nop 0
	global_load_lds_dwordx4 v210, s[20:21]
	s_nop 0
	s_mov_b32 m0, s30
	s_nop 0
	global_load_lds_dwordx4 v213, s[20:21]
	s_add_u32 s26, s20, 0x20000
	s_addc_u32 s27, s21, 0
	s_mov_b32 m0, s31
	s_nop 0
	global_load_lds_dwordx4 v210, s[26:27]
	s_and_b64 vcc, exec, s[24:25]
	s_mov_b32 m0, s34
	s_nop 0
	global_load_lds_dwordx4 v213, s[26:27]
	s_mov_b32 m0, s28
	s_nop 0
	global_load_lds_dwordx4 v226, s[22:23]
	s_nop 0
	s_mov_b32 m0, s35
	s_nop 0
	global_load_lds_dwordx4 v227, s[22:23]
	s_mov_b64 s[26:27], -1
	s_cbranch_vccz .Lpeel_hgrnin_606
	s_waitcnt vmcnt(8)
	s_mov_b64 s[26:27], 0

.Lpeel_hgrnin_608:
	s_waitcnt lgkmcnt(0)
	v_cndmask_b32_e64 v228, v224, v220, s[0:1]
	v_cndmask_b32_e64 v229, v225, v221, s[0:1]
	s_barrier
	s_setprio 1
	s_waitcnt lgkmcnt(6)
	v_mfma_f32_16x16x128_f8f6f4 v[126:129], v[26:33], v[58:65], 0
	v_mfma_f32_16x16x128_f8f6f4 v[122:125], v[18:25], v[58:65], 0
	s_waitcnt lgkmcnt(4)
	v_mfma_f32_16x16x128_f8f6f4 v[110:113], v[26:33], v[50:57], 0
	v_mfma_f32_16x16x128_f8f6f4 v[106:109], v[18:25], v[50:57], 0
	s_waitcnt lgkmcnt(2)
	v_mfma_f32_16x16x128_f8f6f4 v[94:97], v[26:33], v[42:49], 0
	v_mfma_f32_16x16x128_f8f6f4 v[90:93], v[18:25], v[42:49], 0
	s_waitcnt lgkmcnt(0)
	v_mfma_f32_16x16x128_f8f6f4 v[78:81], v[26:33], v[34:41], 0
	v_mfma_f32_16x16x128_f8f6f4 v[74:77], v[18:25], v[34:41], 0
	s_setprio 0
	s_setprio 1
	v_mfma_f32_16x16x128_f8f6f4 v[118:121], v[10:17], v[58:65], 0
	v_mfma_f32_16x16x128_f8f6f4 v[114:117], v[2:9], v[58:65], 0
	v_mfma_f32_16x16x128_f8f6f4 v[102:105], v[10:17], v[50:57], 0
	v_mfma_f32_16x16x128_f8f6f4 v[98:101], v[2:9], v[50:57], 0
	v_mfma_f32_16x16x128_f8f6f4 v[86:89], v[10:17], v[42:49], 0
	v_mfma_f32_16x16x128_f8f6f4 v[82:85], v[2:9], v[42:49], 0
	v_mfma_f32_16x16x128_f8f6f4 v[70:73], v[10:17], v[34:41], 0
	v_mfma_f32_16x16x128_f8f6f4 v[66:69], v[2:9], v[34:41], 0
	s_setprio 0
	s_barrier
	s_branch .Lmid_hgrnin

.LBB0_964:
	s_cmp_lg_u32 s16, 0
	s_cselect_b64 s[16:17], -1, 0
	s_add_u32 s13, s0, 0x100
	s_addc_u32 s51, s1, 0
	s_mov_b32 s52, -2
	s_mov_b64 s[18:19], 0
	v_add_u32_e32 v2, 0x10000, v216
	v_add_u32_e32 v6, 0x14000, v216
	ds_read_b128 v[26:29], v2
	ds_read_b128 v[30:33], v2 offset:1024
	ds_read_b128 v[18:21], v2 offset:2048
	ds_read_b128 v[22:25], v2 offset:3072
	ds_read_b128 v[10:13], v6
	ds_read_b128 v[14:17], v6 offset:1024
	ds_read_b128 v[2:5], v6 offset:2048
	ds_read_b128 v[6:9], v6 offset:3072
	s_add_u32 s22, s2, s18
	s_addc_u32 s23, s3, s19
	s_cmp_eq_u32 s18, 0
	s_cselect_b64 s[0:1], -1, 0
	ds_read_b128 v[58:61], v217
	ds_read_b128 v[62:65], v217 offset:1024
	ds_read_b128 v[50:53], v217 offset:2048
	ds_read_b128 v[54:57], v217 offset:3072
	ds_read_b128 v[42:45], v217 offset:4096
	ds_read_b128 v[46:49], v217 offset:5120
	ds_read_b128 v[34:37], v217 offset:6144
	ds_read_b128 v[38:41], v217 offset:7168
	s_and_b64 s[0:1], s[16:17], s[0:1]
	s_mov_b64 s[20:21], -1
	s_and_b64 vcc, exec, s[0:1]
	s_cbranch_vccnz .Lpeel_poolin_968
	s_add_u32 s20, s22, 0x80
	s_addc_u32 s21, s23, 0
	s_mov_b32 m0, s44
	s_nop 0
	global_load_lds_dwordx4 v224, s[20:21]
	s_nop 0
	s_mov_b32 m0, s45
	s_nop 0
	global_load_lds_dwordx4 v225, s[20:21]
	s_waitcnt vmcnt(8)
	s_mov_b64 s[20:21], 0

.Lpeel_poolin_970:
	s_xor_b64 s[24:25], s[0:1], -1
	s_add_u32 s22, s22, 0x100
	s_addc_u32 s23, s23, 0
	s_add_u32 s26, s13, s18
	s_addc_u32 s27, s51, s19
	s_cmpk_eq_i32 s18, 0x300
	s_cselect_b64 s[0:1], -1, 0
	s_waitcnt lgkmcnt(0)
	s_and_b64 s[20:21], s[0:1], exec
	v_cndmask_b32_e64 v226, v222, v218, s[0:1]
	s_cselect_b32 s23, s3, s23
	s_cselect_b32 s22, s2, s22
	v_cndmask_b32_e64 v227, v223, v219, s[0:1]
	s_cselect_b32 s21, s11, s27
	s_cselect_b32 s20, s10, s26
	s_barrier
	s_setprio 1
	s_waitcnt lgkmcnt(6)
	v_mfma_f32_16x16x128_f8f6f4 v[190:193], v[26:33], v[58:65], 0
	v_mfma_f32_16x16x128_f8f6f4 v[186:189], v[18:25], v[58:65], 0
	s_waitcnt lgkmcnt(4)
	v_mfma_f32_16x16x128_f8f6f4 v[178:181], v[26:33], v[50:57], 0
	v_mfma_f32_16x16x128_f8f6f4 v[170:173], v[18:25], v[50:57], 0
	s_waitcnt lgkmcnt(2)
	v_mfma_f32_16x16x128_f8f6f4 v[162:165], v[26:33], v[42:49], 0
	v_mfma_f32_16x16x128_f8f6f4 v[154:157], v[18:25], v[42:49], 0
	s_waitcnt lgkmcnt(0)
	v_mfma_f32_16x16x128_f8f6f4 v[142:145], v[26:33], v[34:41], 0
	v_mfma_f32_16x16x128_f8f6f4 v[138:141], v[18:25], v[34:41], 0
	s_setprio 0
	s_setprio 1
	v_mfma_f32_16x16x128_f8f6f4 v[182:185], v[10:17], v[58:65], 0
	v_mfma_f32_16x16x128_f8f6f4 v[174:177], v[2:9], v[58:65], 0
	v_mfma_f32_16x16x128_f8f6f4 v[166:169], v[10:17], v[50:57], 0
	v_mfma_f32_16x16x128_f8f6f4 v[158:161], v[2:9], v[50:57], 0
	v_mfma_f32_16x16x128_f8f6f4 v[150:153], v[10:17], v[42:49], 0
	v_mfma_f32_16x16x128_f8f6f4 v[146:149], v[2:9], v[42:49], 0
	v_mfma_f32_16x16x128_f8f6f4 v[134:137], v[10:17], v[34:41], 0
	v_mfma_f32_16x16x128_f8f6f4 v[130:133], v[2:9], v[34:41], 0
	s_setprio 0
	s_barrier
	ds_read_b128 v[58:61], v217 offset:16384
	ds_read_b128 v[62:65], v217 offset:17408
	ds_read_b128 v[50:53], v217 offset:18432
	ds_read_b128 v[54:57], v217 offset:19456
	ds_read_b128 v[42:45], v217 offset:20480
	ds_read_b128 v[46:49], v217 offset:21504
	ds_read_b128 v[34:37], v217 offset:22528
	ds_read_b128 v[38:41], v217 offset:23552
	s_mov_b32 m0, s29
	s_nop 0
	global_load_lds_dwordx4 v210, s[20:21]
	s_nop 0
	s_mov_b32 m0, s30
	s_nop 0
	global_load_lds_dwordx4 v213, s[20:21]
	s_add_u32 s26, s20, 0x20000
	s_addc_u32 s27, s21, 0
	s_mov_b32 m0, s31
	s_nop 0
	global_load_lds_dwordx4 v210, s[26:27]
	s_and_b64 vcc, exec, s[24:25]
	s_mov_b32 m0, s34
	s_nop 0
	global_load_lds_dwordx4 v213, s[26:27]
	s_mov_b32 m0, s28
	s_nop 0
	global_load_lds_dwordx4 v226, s[22:23]
	s_nop 0
	s_mov_b32 m0, s35
	s_nop 0
	global_load_lds_dwordx4 v227, s[22:23]
	s_mov_b64 s[26:27], -1
	s_cbranch_vccz .Lpeel_poolin_972
	s_waitcnt vmcnt(8)
	s_mov_b64 s[26:27], 0

.Lpeel_poolin_974:
	s_waitcnt lgkmcnt(0)
	v_cndmask_b32_e64 v228, v224, v220, s[0:1]
	v_cndmask_b32_e64 v229, v225, v221, s[0:1]
	s_barrier
	s_setprio 1
	s_waitcnt lgkmcnt(6)
	v_mfma_f32_16x16x128_f8f6f4 v[126:129], v[26:33], v[58:65], 0
	v_mfma_f32_16x16x128_f8f6f4 v[122:125], v[18:25], v[58:65], 0
	s_waitcnt lgkmcnt(4)
	v_mfma_f32_16x16x128_f8f6f4 v[114:117], v[26:33], v[50:57], 0
	v_mfma_f32_16x16x128_f8f6f4 v[106:109], v[18:25], v[50:57], 0
	s_waitcnt lgkmcnt(2)
	v_mfma_f32_16x16x128_f8f6f4 v[82:85], v[26:33], v[42:49], 0
	v_mfma_f32_16x16x128_f8f6f4 v[78:81], v[18:25], v[42:49], 0
	s_waitcnt lgkmcnt(0)
	v_mfma_f32_16x16x128_f8f6f4 v[70:73], v[26:33], v[34:41], 0
	v_mfma_f32_16x16x128_f8f6f4 v[66:69], v[18:25], v[34:41], 0
	s_setprio 0
	s_setprio 1
	v_mfma_f32_16x16x128_f8f6f4 v[118:121], v[10:17], v[58:65], 0
	v_mfma_f32_16x16x128_f8f6f4 v[110:113], v[2:9], v[58:65], 0
	v_mfma_f32_16x16x128_f8f6f4 v[86:89], v[10:17], v[50:57], 0
	v_mfma_f32_16x16x128_f8f6f4 v[74:77], v[2:9], v[50:57], 0
	v_mfma_f32_16x16x128_f8f6f4 v[102:105], v[10:17], v[42:49], 0
	v_mfma_f32_16x16x128_f8f6f4 v[98:101], v[2:9], v[42:49], 0
	v_mfma_f32_16x16x128_f8f6f4 v[94:97], v[10:17], v[34:41], 0
	v_mfma_f32_16x16x128_f8f6f4 v[90:93], v[2:9], v[34:41], 0
	s_setprio 0
	s_barrier
	s_branch .Lmid_poolin

.LBB0_1143:
	s_cmp_lg_u32 s22, 0
	s_cselect_b64 s[22:23], -1, 0
	s_add_u32 s19, s4, 0x100
	s_waitcnt vmcnt(9)
	s_addc_u32 s59, s5, 0
	s_mov_b32 s60, -2
	s_mov_b64 s[24:25], 0
	s_waitcnt vmcnt(8)
	s_waitcnt vmcnt(1)
	s_waitcnt vmcnt(0)
	v_add_u32_e32 v2, 0x10000, v216
	v_add_u32_e32 v6, 0x14000, v216
	ds_read_b128 v[26:29], v2
	ds_read_b128 v[30:33], v2 offset:1024
	ds_read_b128 v[18:21], v2 offset:2048
	ds_read_b128 v[22:25], v2 offset:3072
	ds_read_b128 v[10:13], v6
	ds_read_b128 v[14:17], v6 offset:1024
	ds_read_b128 v[2:5], v6 offset:2048
	ds_read_b128 v[6:9], v6 offset:3072
	s_add_u32 s28, s8, s24
	s_addc_u32 s29, s9, s25
	s_cmp_eq_u32 s24, 0
	s_cselect_b64 s[4:5], -1, 0
	ds_read_b128 v[58:61], v217
	ds_read_b128 v[62:65], v217 offset:1024
	ds_read_b128 v[50:53], v217 offset:2048
	ds_read_b128 v[54:57], v217 offset:3072
	ds_read_b128 v[42:45], v217 offset:4096
	ds_read_b128 v[46:49], v217 offset:5120
	ds_read_b128 v[34:37], v217 offset:6144
	ds_read_b128 v[38:41], v217 offset:7168
	s_and_b64 s[4:5], s[22:23], s[4:5]
	s_mov_b64 s[26:27], -1
	s_and_b64 vcc, exec, s[4:5]
	s_cbranch_vccnz .Lpeel_outp_1147
	s_add_u32 s26, s28, 0x80
	s_addc_u32 s27, s29, 0
	s_mov_b32 m0, s53
	s_nop 0
	global_load_lds_dwordx4 v224, s[26:27]
	s_nop 0
	s_mov_b32 m0, s54
	s_nop 0
	global_load_lds_dwordx4 v225, s[26:27]
	s_waitcnt vmcnt(8)
	s_mov_b64 s[26:27], 0

.Lpeel_outp_1149:
	s_xor_b64 s[30:31], s[4:5], -1
	s_add_u32 s28, s28, 0x100
	s_addc_u32 s29, s29, 0
	s_add_u32 s34, s19, s24
	s_addc_u32 s35, s59, s25
	s_cmpk_eq_i32 s24, 0x300
	s_cselect_b64 s[4:5], -1, 0
	s_waitcnt lgkmcnt(0)
	s_and_b64 s[26:27], s[4:5], exec
	v_cndmask_b32_e64 v226, v222, v218, s[4:5]
	s_cselect_b32 s29, s9, s29
	s_cselect_b32 s28, s8, s28
	v_cndmask_b32_e64 v227, v223, v219, s[4:5]
	s_cselect_b32 s27, s17, s35
	s_cselect_b32 s26, s16, s34
	s_barrier
	s_setprio 1
	s_waitcnt lgkmcnt(6)
	v_mfma_f32_16x16x128_f8f6f4 v[190:193], v[26:33], v[58:65], 0
	v_mfma_f32_16x16x128_f8f6f4 v[186:189], v[18:25], v[58:65], 0
	s_waitcnt lgkmcnt(4)
	v_mfma_f32_16x16x128_f8f6f4 v[178:181], v[26:33], v[50:57], 0
	v_mfma_f32_16x16x128_f8f6f4 v[170:173], v[18:25], v[50:57], 0
	s_waitcnt lgkmcnt(2)
	v_mfma_f32_16x16x128_f8f6f4 v[158:161], v[26:33], v[42:49], 0
	v_mfma_f32_16x16x128_f8f6f4 v[154:157], v[18:25], v[42:49], 0
	s_waitcnt lgkmcnt(0)
	v_mfma_f32_16x16x128_f8f6f4 v[142:145], v[26:33], v[34:41], 0
	v_mfma_f32_16x16x128_f8f6f4 v[138:141], v[18:25], v[34:41], 0
	s_setprio 0
	s_setprio 1
	v_mfma_f32_16x16x128_f8f6f4 v[182:185], v[10:17], v[58:65], 0
	v_mfma_f32_16x16x128_f8f6f4 v[174:177], v[2:9], v[58:65], 0
	v_mfma_f32_16x16x128_f8f6f4 v[166:169], v[10:17], v[50:57], 0
	v_mfma_f32_16x16x128_f8f6f4 v[162:165], v[2:9], v[50:57], 0
	v_mfma_f32_16x16x128_f8f6f4 v[150:153], v[10:17], v[42:49], 0
	v_mfma_f32_16x16x128_f8f6f4 v[146:149], v[2:9], v[42:49], 0
	v_mfma_f32_16x16x128_f8f6f4 v[134:137], v[10:17], v[34:41], 0
	v_mfma_f32_16x16x128_f8f6f4 v[130:133], v[2:9], v[34:41], 0
	s_setprio 0
	s_barrier
	ds_read_b128 v[58:61], v217 offset:16384
	ds_read_b128 v[62:65], v217 offset:17408
	ds_read_b128 v[50:53], v217 offset:18432
	ds_read_b128 v[54:57], v217 offset:19456
	ds_read_b128 v[42:45], v217 offset:20480
	ds_read_b128 v[46:49], v217 offset:21504
	ds_read_b128 v[34:37], v217 offset:22528
	ds_read_b128 v[38:41], v217 offset:23552
	s_mov_b32 m0, s37
	s_nop 0
	global_load_lds_dwordx4 v210, s[26:27]
	s_nop 0
	s_mov_b32 m0, s38
	s_nop 0
	global_load_lds_dwordx4 v213, s[26:27]
	s_add_u32 s34, s26, 0x20000
	s_addc_u32 s35, s27, 0
	s_mov_b32 m0, s39
	s_nop 0
	global_load_lds_dwordx4 v210, s[34:35]
	s_and_b64 vcc, exec, s[30:31]
	s_mov_b32 m0, s40
	s_nop 0
	global_load_lds_dwordx4 v213, s[34:35]
	s_mov_b32 m0, s36
	s_nop 0
	global_load_lds_dwordx4 v226, s[28:29]
	s_nop 0
	s_mov_b32 m0, s41
	s_nop 0
	global_load_lds_dwordx4 v227, s[28:29]
	s_mov_b64 s[34:35], -1
	s_cbranch_vccz .Lpeel_outp_1151
	s_waitcnt vmcnt(8)
	s_mov_b64 s[34:35], 0

.Lpeel_outp_1153:
	s_waitcnt lgkmcnt(0)
	v_cndmask_b32_e64 v228, v224, v220, s[4:5]
	v_cndmask_b32_e64 v229, v225, v221, s[4:5]
	s_barrier
	s_setprio 1
	s_waitcnt lgkmcnt(6)
	v_mfma_f32_16x16x128_f8f6f4 v[126:129], v[26:33], v[58:65], 0
	v_mfma_f32_16x16x128_f8f6f4 v[122:125], v[18:25], v[58:65], 0
	s_waitcnt lgkmcnt(4)
	v_mfma_f32_16x16x128_f8f6f4 v[110:113], v[26:33], v[50:57], 0
	v_mfma_f32_16x16x128_f8f6f4 v[106:109], v[18:25], v[50:57], 0
	s_waitcnt lgkmcnt(2)
	v_mfma_f32_16x16x128_f8f6f4 v[86:89], v[26:33], v[42:49], 0
	v_mfma_f32_16x16x128_f8f6f4 v[82:85], v[18:25], v[42:49], 0
	s_waitcnt lgkmcnt(0)
	v_mfma_f32_16x16x128_f8f6f4 v[70:73], v[26:33], v[34:41], 0
	v_mfma_f32_16x16x128_f8f6f4 v[66:69], v[18:25], v[34:41], 0
	s_setprio 0
	s_setprio 1
	v_mfma_f32_16x16x128_f8f6f4 v[118:121], v[10:17], v[58:65], 0
	v_mfma_f32_16x16x128_f8f6f4 v[114:117], v[2:9], v[58:65], 0
	v_mfma_f32_16x16x128_f8f6f4 v[94:97], v[10:17], v[50:57], 0
	v_mfma_f32_16x16x128_f8f6f4 v[90:93], v[2:9], v[50:57], 0
	v_mfma_f32_16x16x128_f8f6f4 v[102:105], v[10:17], v[42:49], 0
	v_mfma_f32_16x16x128_f8f6f4 v[98:101], v[2:9], v[42:49], 0
	v_mfma_f32_16x16x128_f8f6f4 v[78:81], v[10:17], v[34:41], 0
	v_mfma_f32_16x16x128_f8f6f4 v[74:77], v[2:9], v[34:41], 0
	s_setprio 0
	s_barrier
	s_branch .Lmid_outp

.Lmid_outp:
	v_add_u32_e32 v2, 0x18000, v216
	v_add_u32_e32 v6, 0x1c000, v216
	ds_read_b128 v[26:29], v2
	ds_read_b128 v[30:33], v2 offset:1024
	ds_read_b128 v[18:21], v2 offset:2048
	ds_read_b128 v[22:25], v2 offset:3072
	ds_read_b128 v[10:13], v6
	ds_read_b128 v[14:17], v6 offset:1024
	ds_read_b128 v[2:5], v6 offset:2048
	ds_read_b128 v[6:9], v6 offset:3072
	ds_read_b128 v[58:61], v217 offset:32768
	ds_read_b128 v[62:65], v217 offset:33792
	ds_read_b128 v[50:53], v217 offset:34816
	ds_read_b128 v[54:57], v217 offset:35840
	ds_read_b128 v[42:45], v217 offset:36864
	ds_read_b128 v[46:49], v217 offset:37888
	ds_read_b128 v[34:37], v217 offset:38912
	ds_read_b128 v[38:41], v217 offset:39936
	s_mov_b32 m0, s42
	s_nop 0
	global_load_lds_dwordx4 v228, s[28:29]
	s_and_b64 vcc, exec, s[30:31]
	s_mov_b32 m0, s43
	s_nop 0
	global_load_lds_dwordx4 v229, s[28:29]
	s_mov_b64 s[4:5], -1
	s_cbranch_vccz .LBB0_1155
	s_waitcnt vmcnt(8)
	s_mov_b64 s[4:5], 0

.LBB0_1641:
	s_cmp_lg_u32 s18, 0
	s_cselect_b64 s[18:19], -1, 0
	s_add_u32 s15, s4, 0x100
	s_addc_u32 s54, s5, 0
	s_mov_b32 s55, -2
	s_mov_b64 s[20:21], 0
	v_add_u32_e32 v2, 0x10000, v217
	v_add_u32_e32 v6, 0x14000, v217
	ds_read_b128 v[26:29], v2
	ds_read_b128 v[30:33], v2 offset:1024
	ds_read_b128 v[18:21], v2 offset:2048
	ds_read_b128 v[22:25], v2 offset:3072
	ds_read_b128 v[10:13], v6
	ds_read_b128 v[14:17], v6 offset:1024
	ds_read_b128 v[2:5], v6 offset:2048
	ds_read_b128 v[6:9], v6 offset:3072
	s_add_u32 s24, s2, s20
	s_addc_u32 s25, s3, s21
	s_cmp_eq_u32 s20, 0
	s_cselect_b64 s[4:5], -1, 0
	ds_read_b128 v[58:61], v218
	ds_read_b128 v[62:65], v218 offset:1024
	ds_read_b128 v[50:53], v218 offset:2048
	ds_read_b128 v[54:57], v218 offset:3072
	ds_read_b128 v[42:45], v218 offset:4096
	ds_read_b128 v[46:49], v218 offset:5120
	ds_read_b128 v[34:37], v218 offset:6144
	ds_read_b128 v[38:41], v218 offset:7168
	s_and_b64 s[4:5], s[18:19], s[4:5]
	s_mov_b64 s[22:23], -1
	s_and_b64 vcc, exec, s[4:5]
	s_cbranch_vccnz .Lpeel_gu_1645
	s_add_u32 s22, s24, 0x80
	s_addc_u32 s23, s25, 0
	s_mov_b32 m0, s47
	s_nop 0
	global_load_lds_dwordx4 v224, s[22:23]
	s_nop 0
	s_mov_b32 m0, s48
	s_nop 0
	global_load_lds_dwordx4 v225, s[22:23]
	s_waitcnt vmcnt(8)
	s_mov_b64 s[22:23], 0

.Lpeel_gu_1647:
	s_xor_b64 s[26:27], s[4:5], -1
	s_add_u32 s24, s24, 0x100
	s_addc_u32 s25, s25, 0
	s_add_u32 s28, s15, s20
	s_addc_u32 s29, s54, s21
	s_cmpk_eq_i32 s20, 0x300
	s_cselect_b64 s[4:5], -1, 0
	s_waitcnt lgkmcnt(0)
	s_and_b64 s[22:23], s[4:5], exec
	v_cndmask_b32_e64 v194, v226, v220, s[4:5]
	s_cselect_b32 s25, s3, s25
	s_cselect_b32 s24, s2, s24
	v_cndmask_b32_e64 v227, v223, v219, s[4:5]
	s_cselect_b32 s23, s17, s29
	s_cselect_b32 s22, s16, s28
	s_barrier
	s_setprio 1
	s_waitcnt lgkmcnt(6)
	v_mfma_f32_16x16x128_f8f6f4 v[190:193], v[26:33], v[58:65], 0
	v_mfma_f32_16x16x128_f8f6f4 v[186:189], v[18:25], v[58:65], 0
	s_waitcnt lgkmcnt(4)
	v_mfma_f32_16x16x128_f8f6f4 v[174:177], v[26:33], v[50:57], 0
	v_mfma_f32_16x16x128_f8f6f4 v[170:173], v[18:25], v[50:57], 0
	s_waitcnt lgkmcnt(2)
	v_mfma_f32_16x16x128_f8f6f4 v[158:161], v[26:33], v[42:49], 0
	v_mfma_f32_16x16x128_f8f6f4 v[154:157], v[18:25], v[42:49], 0
	s_waitcnt lgkmcnt(0)
	v_mfma_f32_16x16x128_f8f6f4 v[142:145], v[26:33], v[34:41], 0
	v_mfma_f32_16x16x128_f8f6f4 v[138:141], v[18:25], v[34:41], 0
	s_setprio 0
	s_setprio 1
	v_mfma_f32_16x16x128_f8f6f4 v[182:185], v[10:17], v[58:65], 0
	v_mfma_f32_16x16x128_f8f6f4 v[178:181], v[2:9], v[58:65], 0
	v_mfma_f32_16x16x128_f8f6f4 v[166:169], v[10:17], v[50:57], 0
	v_mfma_f32_16x16x128_f8f6f4 v[162:165], v[2:9], v[50:57], 0
	v_mfma_f32_16x16x128_f8f6f4 v[150:153], v[10:17], v[42:49], 0
	v_mfma_f32_16x16x128_f8f6f4 v[146:149], v[2:9], v[42:49], 0
	v_mfma_f32_16x16x128_f8f6f4 v[134:137], v[10:17], v[34:41], 0
	v_mfma_f32_16x16x128_f8f6f4 v[130:133], v[2:9], v[34:41], 0
	s_setprio 0
	s_barrier
	ds_read_b128 v[58:61], v218 offset:16384
	ds_read_b128 v[62:65], v218 offset:17408
	ds_read_b128 v[50:53], v218 offset:18432
	ds_read_b128 v[54:57], v218 offset:19456
	ds_read_b128 v[42:45], v218 offset:20480
	ds_read_b128 v[46:49], v218 offset:21504
	ds_read_b128 v[34:37], v218 offset:22528
	ds_read_b128 v[38:41], v218 offset:23552
	s_mov_b32 m0, s31
	s_nop 0
	global_load_lds_dwordx4 v210, s[22:23]
	s_nop 0
	s_mov_b32 m0, s34
	s_nop 0
	global_load_lds_dwordx4 v212, s[22:23]
	s_add_u32 s28, s22, 0x20000
	s_addc_u32 s29, s23, 0
	s_mov_b32 m0, s35
	s_nop 0
	global_load_lds_dwordx4 v210, s[28:29]
	s_and_b64 vcc, exec, s[26:27]
	s_mov_b32 m0, s36
	s_nop 0
	global_load_lds_dwordx4 v212, s[28:29]
	s_mov_b32 m0, s30
	s_nop 0
	global_load_lds_dwordx4 v194, s[24:25]
	s_nop 0
	s_mov_b32 m0, s37
	s_nop 0
	global_load_lds_dwordx4 v227, s[24:25]
	s_mov_b64 s[28:29], -1
	s_cbranch_vccz .Lpeel_gu_1649
	s_waitcnt vmcnt(8)
	s_mov_b64 s[28:29], 0

.Lpeel_gu_1651:
	s_waitcnt lgkmcnt(0)
	v_cndmask_b32_e64 v228, v224, v221, s[4:5]
	v_cndmask_b32_e64 v229, v225, v222, s[4:5]
	s_barrier
	s_setprio 1
	s_waitcnt lgkmcnt(6)
	v_mfma_f32_16x16x128_f8f6f4 v[126:129], v[26:33], v[58:65], 0
	v_mfma_f32_16x16x128_f8f6f4 v[122:125], v[18:25], v[58:65], 0
	s_waitcnt lgkmcnt(4)
	v_mfma_f32_16x16x128_f8f6f4 v[110:113], v[26:33], v[50:57], 0
	v_mfma_f32_16x16x128_f8f6f4 v[106:109], v[18:25], v[50:57], 0
	s_waitcnt lgkmcnt(2)
	v_mfma_f32_16x16x128_f8f6f4 v[86:89], v[26:33], v[42:49], 0
	v_mfma_f32_16x16x128_f8f6f4 v[82:85], v[18:25], v[42:49], 0
	s_waitcnt lgkmcnt(0)
	v_mfma_f32_16x16x128_f8f6f4 v[70:73], v[26:33], v[34:41], 0
	v_mfma_f32_16x16x128_f8f6f4 v[66:69], v[18:25], v[34:41], 0
	s_setprio 0
	s_setprio 1
	v_mfma_f32_16x16x128_f8f6f4 v[118:121], v[10:17], v[58:65], 0
	v_mfma_f32_16x16x128_f8f6f4 v[114:117], v[2:9], v[58:65], 0
	v_mfma_f32_16x16x128_f8f6f4 v[102:105], v[10:17], v[50:57], 0
	v_mfma_f32_16x16x128_f8f6f4 v[90:93], v[2:9], v[50:57], 0
	v_mfma_f32_16x16x128_f8f6f4 v[98:101], v[10:17], v[42:49], 0
	v_mfma_f32_16x16x128_f8f6f4 v[94:97], v[2:9], v[42:49], 0
	v_mfma_f32_16x16x128_f8f6f4 v[78:81], v[10:17], v[34:41], 0
	v_mfma_f32_16x16x128_f8f6f4 v[74:77], v[2:9], v[34:41], 0
	s_setprio 0
	s_barrier
	s_branch .Lmid_gu

.Lmid_gu:
	v_add_u32_e32 v2, 0x18000, v217
	v_add_u32_e32 v6, 0x1c000, v217
	ds_read_b128 v[26:29], v2
	ds_read_b128 v[30:33], v2 offset:1024
	ds_read_b128 v[18:21], v2 offset:2048
	ds_read_b128 v[22:25], v2 offset:3072
	ds_read_b128 v[10:13], v6
	ds_read_b128 v[14:17], v6 offset:1024
	ds_read_b128 v[2:5], v6 offset:2048
	ds_read_b128 v[6:9], v6 offset:3072
	ds_read_b128 v[58:61], v218 offset:32768
	ds_read_b128 v[62:65], v218 offset:33792
	ds_read_b128 v[50:53], v218 offset:34816
	ds_read_b128 v[54:57], v218 offset:35840
	ds_read_b128 v[42:45], v218 offset:36864
	ds_read_b128 v[46:49], v218 offset:37888
	ds_read_b128 v[34:37], v218 offset:38912
	ds_read_b128 v[38:41], v218 offset:39936
	s_mov_b32 m0, s38
	s_nop 0
	global_load_lds_dwordx4 v228, s[24:25]
	s_and_b64 vcc, exec, s[26:27]
	s_mov_b32 m0, s39
	s_nop 0
	global_load_lds_dwordx4 v229, s[24:25]
	s_mov_b64 s[4:5], -1
	s_cbranch_vccz .LBB0_1653
	s_waitcnt vmcnt(8)
	s_mov_b64 s[4:5], 0

.LBB0_1796:
	s_cmp_lg_u32 s52, 0
	s_cselect_b64 s[18:19], -1, 0
	s_add_u32 s15, s4, 0x100
	s_addc_u32 s53, s5, 0
	s_mov_b32 s54, -2
	s_mov_b64 s[20:21], 0
	v_add_u32_e32 v2, 0x10000, v217
	v_add_u32_e32 v6, 0x14000, v217
	ds_read_b128 v[26:29], v2
	ds_read_b128 v[30:33], v2 offset:1024
	ds_read_b128 v[18:21], v2 offset:2048
	ds_read_b128 v[22:25], v2 offset:3072
	ds_read_b128 v[10:13], v6
	ds_read_b128 v[14:17], v6 offset:1024
	ds_read_b128 v[2:5], v6 offset:2048
	ds_read_b128 v[6:9], v6 offset:3072
	v_readlane_b32 s4, v246, 11
	v_readlane_b32 s5, v246, 12
	s_add_u32 s24, s4, s20
	s_addc_u32 s25, s5, s21
	s_cmp_eq_u32 s20, 0
	s_cselect_b64 s[4:5], -1, 0
	ds_read_b128 v[58:61], v218
	ds_read_b128 v[62:65], v218 offset:1024
	ds_read_b128 v[50:53], v218 offset:2048
	ds_read_b128 v[54:57], v218 offset:3072
	ds_read_b128 v[42:45], v218 offset:4096
	ds_read_b128 v[46:49], v218 offset:5120
	ds_read_b128 v[34:37], v218 offset:6144
	ds_read_b128 v[38:41], v218 offset:7168
	s_and_b64 s[4:5], s[18:19], s[4:5]
	s_mov_b64 s[22:23], -1
	s_and_b64 vcc, exec, s[4:5]
	s_cbranch_vccnz .Lpeel_dn_1800
	s_add_u32 s22, s24, 0x80
	s_addc_u32 s23, s25, 0
	s_mov_b32 m0, s47
	s_nop 0
	global_load_lds_dwordx4 v224, s[22:23]
	s_nop 0
	s_mov_b32 m0, s48
	s_nop 0
	global_load_lds_dwordx4 v225, s[22:23]
	s_waitcnt vmcnt(8)
	s_mov_b64 s[22:23], 0

.Lpeel_dn_1802:
	s_xor_b64 s[26:27], s[4:5], -1
	s_add_u32 s24, s24, 0x100
	s_addc_u32 s25, s25, 0
	s_add_u32 s28, s15, s20
	s_addc_u32 s29, s53, s21
	s_cmpk_eq_i32 s20, 0x300
	s_cselect_b64 s[4:5], -1, 0
	s_and_b64 s[22:23], s[4:5], exec
	v_readlane_b32 s22, v246, 11
	s_waitcnt lgkmcnt(0)
	v_readlane_b32 s23, v246, 12
	v_cndmask_b32_e64 v194, v226, v221, s[4:5]
	s_cselect_b32 s25, s23, s25
	s_cselect_b32 s24, s22, s24
	v_cndmask_b32_e64 v227, v223, v219, s[4:5]
	s_cselect_b32 s23, s17, s29
	s_cselect_b32 s22, s16, s28
	s_barrier
	s_setprio 1
	s_waitcnt lgkmcnt(6)
	v_mfma_f32_16x16x128_f8f6f4 v[190:193], v[26:33], v[58:65], 0
	v_mfma_f32_16x16x128_f8f6f4 v[186:189], v[18:25], v[58:65], 0
	s_waitcnt lgkmcnt(4)
	v_mfma_f32_16x16x128_f8f6f4 v[174:177], v[26:33], v[50:57], 0
	v_mfma_f32_16x16x128_f8f6f4 v[170:173], v[18:25], v[50:57], 0
	s_waitcnt lgkmcnt(2)
	v_mfma_f32_16x16x128_f8f6f4 v[158:161], v[26:33], v[42:49], 0
	v_mfma_f32_16x16x128_f8f6f4 v[154:157], v[18:25], v[42:49], 0
	s_waitcnt lgkmcnt(0)
	v_mfma_f32_16x16x128_f8f6f4 v[142:145], v[26:33], v[34:41], 0
	v_mfma_f32_16x16x128_f8f6f4 v[138:141], v[18:25], v[34:41], 0
	s_setprio 0
	s_setprio 1
	v_mfma_f32_16x16x128_f8f6f4 v[182:185], v[10:17], v[58:65], 0
	v_mfma_f32_16x16x128_f8f6f4 v[178:181], v[2:9], v[58:65], 0
	v_mfma_f32_16x16x128_f8f6f4 v[166:169], v[10:17], v[50:57], 0
	v_mfma_f32_16x16x128_f8f6f4 v[162:165], v[2:9], v[50:57], 0
	v_mfma_f32_16x16x128_f8f6f4 v[150:153], v[10:17], v[42:49], 0
	v_mfma_f32_16x16x128_f8f6f4 v[146:149], v[2:9], v[42:49], 0
	v_mfma_f32_16x16x128_f8f6f4 v[134:137], v[10:17], v[34:41], 0
	v_mfma_f32_16x16x128_f8f6f4 v[130:133], v[2:9], v[34:41], 0
	s_setprio 0
	s_barrier
	ds_read_b128 v[58:61], v218 offset:16384
	ds_read_b128 v[62:65], v218 offset:17408
	ds_read_b128 v[50:53], v218 offset:18432
	ds_read_b128 v[54:57], v218 offset:19456
	ds_read_b128 v[42:45], v218 offset:20480
	ds_read_b128 v[46:49], v218 offset:21504
	ds_read_b128 v[34:37], v218 offset:22528
	ds_read_b128 v[38:41], v218 offset:23552
	s_mov_b32 m0, s31
	s_nop 0
	global_load_lds_dwordx4 v211, s[22:23]
	s_nop 0
	s_mov_b32 m0, s34
	s_nop 0
	global_load_lds_dwordx4 v214, s[22:23]
	s_add_u32 s28, s22, 0x20000
	s_addc_u32 s29, s23, 0
	s_mov_b32 m0, s35
	s_nop 0
	global_load_lds_dwordx4 v211, s[28:29]
	s_and_b64 vcc, exec, s[26:27]
	s_mov_b32 m0, s36
	s_nop 0
	global_load_lds_dwordx4 v214, s[28:29]
	s_mov_b32 m0, s30
	s_nop 0
	global_load_lds_dwordx4 v194, s[24:25]
	s_nop 0
	s_mov_b32 m0, s37
	s_nop 0
	global_load_lds_dwordx4 v227, s[24:25]
	s_mov_b64 s[28:29], -1
	s_cbranch_vccz .Lpeel_dn_1804
	s_waitcnt vmcnt(8)
	s_mov_b64 s[28:29], 0

.Lpeel_dn_1806:
	s_waitcnt lgkmcnt(0)
	v_cndmask_b32_e64 v228, v224, v220, s[4:5]
	v_cndmask_b32_e64 v229, v225, v222, s[4:5]
	s_barrier
	s_setprio 1
	s_waitcnt lgkmcnt(6)
	v_mfma_f32_16x16x128_f8f6f4 v[126:129], v[26:33], v[58:65], 0
	v_mfma_f32_16x16x128_f8f6f4 v[122:125], v[18:25], v[58:65], 0
	s_waitcnt lgkmcnt(4)
	v_mfma_f32_16x16x128_f8f6f4 v[110:113], v[26:33], v[50:57], 0
	v_mfma_f32_16x16x128_f8f6f4 v[106:109], v[18:25], v[50:57], 0
	s_waitcnt lgkmcnt(2)
	v_mfma_f32_16x16x128_f8f6f4 v[86:89], v[26:33], v[42:49], 0
	v_mfma_f32_16x16x128_f8f6f4 v[74:77], v[18:25], v[42:49], 0
	s_waitcnt lgkmcnt(0)
	v_mfma_f32_16x16x128_f8f6f4 v[70:73], v[26:33], v[34:41], 0
	v_mfma_f32_16x16x128_f8f6f4 v[66:69], v[18:25], v[34:41], 0
	s_setprio 0
	s_setprio 1
	v_mfma_f32_16x16x128_f8f6f4 v[118:121], v[10:17], v[58:65], 0
	v_mfma_f32_16x16x128_f8f6f4 v[114:117], v[2:9], v[58:65], 0
	v_mfma_f32_16x16x128_f8f6f4 v[94:97], v[10:17], v[50:57], 0
	v_mfma_f32_16x16x128_f8f6f4 v[90:93], v[2:9], v[50:57], 0
	v_mfma_f32_16x16x128_f8f6f4 v[102:105], v[10:17], v[42:49], 0
	v_mfma_f32_16x16x128_f8f6f4 v[98:101], v[2:9], v[42:49], 0
	v_mfma_f32_16x16x128_f8f6f4 v[82:85], v[10:17], v[34:41], 0
	v_mfma_f32_16x16x128_f8f6f4 v[78:81], v[2:9], v[34:41], 0
	s_setprio 0
	s_barrier
	s_branch .Lmid_dn
